# speedup vs baseline: 1.0282x; 1.0282x over previous
_Z11proj_kernelPKfS0_S0_PKDF16_S0_S0_S0_PDF16_S3_S3_Pj:
	s_ashr_i32 s12, s2, 6
	s_load_dwordx8 s[4:11], s[0:1], 0x0
	s_cmp_gt_u32 s2, 63
	s_cselect_b64 s[22:23], -1, 0
	s_cmp_lg_u32 s12, 1
	s_cselect_b64 s[18:19], -1, 0
	s_cmp_eq_u32 s12, 1
	s_cselect_b64 s[20:21], -1, 0
	s_and_b64 s[14:15], s[20:21], exec
	s_waitcnt lgkmcnt(0)
	s_cselect_b32 s14, s6, s8
	s_cselect_b32 s15, s7, s9
	s_ashr_i32 s13, s12, 31
	s_lshl_b32 s28, s2, 7
	s_lshl_b64 s[6:7], s[12:13], 19
	s_and_b32 s3, s28, 0x1f80
	s_cmp_lt_u32 s2, 64
	s_cselect_b64 vcc, -1, 0
	v_lshrrev_b32_e32 v1, 2, v0
	v_lshrrev_b32_e32 v2, 2, v0
	v_and_b32_e32 v2, 0x70, v2
	v_bfe_u32 v254, v0, 3, 3
	v_or_b32_e32 v254, v2, v254
	v_or_b32_e32 v2, s3, v254
	s_and_b64 s[8:9], vcc, exec
	s_cselect_b32 s25, s5, s15
	s_cselect_b32 s24, s4, s14
	v_lshlrev_b32_e32 v2, 11, v2
	v_mov_b32_e32 v3, 0
	v_lshlrev_b32_e32 v6, 4, v0
	s_add_u32 s4, s10, s6
	v_lshl_add_u64 v[4:5], s[24:25], 0, v[2:3]
	v_and_b32_e32 v6, 0x70, v6
	v_mov_b32_e32 v7, v3
	v_lshlrev_b32_e32 v56, 4, v0
	v_mov_b32_e32 v57, v3
	s_addc_u32 s5, s11, s7
	v_lshl_add_u64 v[4:5], v[4:5], 0, v[6:7]
	s_mov_b64 s[46:47], 0x4000
	v_lshl_add_u64 v[250:251], v[4:5], 0, s[46:47]
	s_movk_i32 s8, 0x2000
	v_lshl_add_u64 v[6:7], s[4:5], 0, v[56:57]
	global_load_dwordx4 v[8:11], v[4:5], off nt
	global_load_dwordx4 v[12:15], v[250:251], off nt
	global_load_dwordx4 v[16:19], v56, s[4:5] sc1
	v_add_co_u32_e64 v28, s[4:5], s8, v6
	s_mov_b32 s33, 0xa000
	s_nop 0
	v_addc_co_u32_e64 v29, s[4:5], 0, v7, s[4:5]
	s_movk_i32 s4, 0x4000
	s_nop 0
	v_add_co_u32_e64 v30, s[4:5], s4, v6
	s_mov_b32 s6, 0xe000
	s_nop 0
	v_addc_co_u32_e64 v31, s[4:5], 0, v7, s[4:5]
	global_load_dwordx4 v[20:23], v[28:29], off sc1
	global_load_dwordx4 v[24:27], v[30:31], off sc1
	s_movk_i32 s4, 0x6000
	v_add_co_u32_e64 v40, s[4:5], s4, v6
	v_lshlrev_b32_e32 v57, 6, v1
	s_nop 0
	v_addc_co_u32_e64 v41, s[4:5], 0, v7, s[4:5]
	global_load_dwordx4 v[28:31], v[40:41], off sc1
	global_load_dwordx4 v[32:35], v[4:5], off offset:128 nt
	global_load_dwordx4 v[36:39], v[250:251], off offset:128 nt
	s_mov_b32 s4, 0x8000
	v_add_co_u32_e64 v40, s[4:5], s4, v6
	v_bitop3_b32 v58, v56, 48, v0 bitop3:0x48
	s_nop 0
	v_addc_co_u32_e64 v41, s[4:5], 0, v7, s[4:5]
	v_add_co_u32_e64 v44, s[4:5], s33, v6
	global_load_dwordx4 v[40:43], v[40:41], off sc1
	s_nop 0
	v_addc_co_u32_e64 v45, s[4:5], 0, v7, s[4:5]
	s_mov_b32 s4, 0xc000
	s_nop 0
	v_add_co_u32_e64 v48, s[4:5], s4, v6
	global_load_dwordx4 v[44:47], v[44:45], off sc1
	s_nop 0
	v_addc_co_u32_e64 v49, s[4:5], 0, v7, s[4:5]
	v_add_co_u32_e64 v52, s[4:5], s6, v6
	global_load_dwordx4 v[48:51], v[48:49], off sc1
	s_nop 0
	v_addc_co_u32_e64 v53, s[4:5], 0, v7, s[4:5]
	global_load_dwordx4 v[52:55], v[52:53], off sc1
	s_mov_b32 s4, 0x1e000
	v_bfe_u32 v57, v0, 1, 2
	v_bfe_u32 v58, v254, 2, 2
	v_xor_b32_e32 v57, v57, v58
	v_lshlrev_b32_e32 v57, 4, v57
	v_and_b32_e32 v58, 1, v0
	v_lshl_or_b32 v57, v58, 3, v57
	v_lshl_add_u32 v209, v254, 6, v57
	v_xor_b32_e32 v248, 32, v209
	v_add_u32_e32 v248, 0x200, v248
	v_add_u32_e32 v208, 0, v56
	v_readfirstlane_b32 s30, v0
	v_bfe_u32 v207, v0, 5, 1
	v_bitop3_b32 v1, v207, v1, 3 bitop3:0x78
	v_lshlrev_b32_e32 v210, 4, v1
	s_mov_b32 s34, 0x14000
	v_add_u32_e32 v213, 0x2000, v208
	s_mov_b32 s43, 0
	s_lshr_b32 s29, s30, 6
	s_mov_b32 s35, -2
	s_mov_b32 s36, 0xffff2000
	s_mov_b32 s37, 0xffff4000
	s_mov_b32 s38, 0xffff6000
	s_movk_i32 s39, 0x8000
	s_movk_i32 s40, 0xa000
	s_movk_i32 s41, 0xc000
	s_movk_i32 s42, 0xe000
	s_mov_b64 s[26:27], 0x100
	v_mov_b32_e32 v56, v3
	v_mov_b32_e32 v57, v3
	v_mov_b32_e32 v58, v3
	v_mov_b32_e32 v59, v3
	v_mov_b32_e32 v60, v3
	v_mov_b32_e32 v61, v3
	v_mov_b32_e32 v62, v3
	v_mov_b32_e32 v63, v3
	v_mov_b32_e32 v64, v3
	v_mov_b32_e32 v65, v3
	v_mov_b32_e32 v66, v3
	v_mov_b32_e32 v67, v3
	v_mov_b32_e32 v68, v3
	v_mov_b32_e32 v69, v3
	v_mov_b32_e32 v70, v3
	s_waitcnt vmcnt(11)
	v_cvt_pk_f16_f32 v8, v8, v9
	v_cvt_pk_f16_f32 v9, v10, v11
	s_waitcnt vmcnt(10)
	v_cvt_pk_f16_f32 v10, v12, v13
	v_cvt_pk_f16_f32 v11, v14, v15
	ds_write_b64 v209, v[8:9]
	ds_write_b64 v248, v[10:11]
	v_and_b32_e32 v10, 31, v0
	s_waitcnt vmcnt(9)
	ds_write_b128 v208, v[16:19] offset:8192
	s_waitcnt vmcnt(8)
	ds_write_b128 v208, v[20:23] offset:16384
	s_waitcnt vmcnt(7)
	ds_write_b128 v208, v[24:27] offset:24576
	s_load_dwordx2 s[16:17], s[0:1], 0x50
	s_load_dwordx4 s[12:15], s[0:1], 0x40
	s_load_dwordx8 s[4:11], s[0:1], 0x20
	s_lshl_b32 s0, s30, 1
	s_and_b32 s31, s0, 0x180
	s_lshr_b32 s0, s30, 2
	v_bfe_u32 v11, v0, 2, 2
	s_and_b32 s0, s0, 0x3fffffc0
	s_waitcnt vmcnt(5)
	v_cvt_pk_f16_f32 v8, v32, v33
	v_cvt_pk_f16_f32 v9, v34, v35
	v_or_b32_e32 v12, s31, v10
	v_or_b32_e32 v206, s0, v10
	v_bitop3_b32 v1, v207, v11, 2 bitop3:0x36
	s_waitcnt vmcnt(4)
	v_cvt_pk_f16_f32 v10, v36, v37
	v_cvt_pk_f16_f32 v11, v38, v39
	s_mov_b32 s0, 0x10000
	ds_write_b128 v208, v[28:31] offset:32768
	ds_write_b64 v209, v[8:9] offset:40960
	ds_write_b64 v248, v[10:11] offset:40960
	v_add_co_u32_e64 v8, s[0:1], s0, v6
	global_load_dwordx4 v[154:157], v[250:251], off offset:256 nt
	global_load_dwordx4 v[162:165], v[4:5], off offset:256 nt
	v_addc_co_u32_e64 v9, s[0:1], 0, v7, s[0:1]
	s_mov_b32 s0, 0x12000
	global_load_dwordx4 v[158:161], v[8:9], off sc1
	v_add_co_u32_e64 v8, s[0:1], s0, v6
	v_lshl_add_u32 v211, v12, 6, 0
	s_nop 0
	v_addc_co_u32_e64 v9, s[0:1], 0, v7, s[0:1]
	v_add_co_u32_e64 v10, s[0:1], s34, v6
	v_add_u32_e32 v14, 0x12000, v208
	s_nop 0
	v_addc_co_u32_e64 v11, s[0:1], 0, v7, s[0:1]
	s_mov_b32 s0, 0x16000
	s_nop 0
	v_add_co_u32_e64 v12, s[0:1], s0, v6
	s_waitcnt vmcnt(3)
	ds_write_b128 v14, v[52:55]
	v_addc_co_u32_e64 v13, s[0:1], 0, v7, s[0:1]
	s_mov_b32 s0, 0x18000
	s_nop 0
	v_add_co_u32_e64 v14, s[0:1], s0, v6
	ds_write_b128 v208, v[40:43] offset:49152
	s_nop 0
	v_addc_co_u32_e64 v15, s[0:1], 0, v7, s[0:1]
	s_mov_b32 s0, 0x1a000
	s_nop 0
	v_add_co_u32_e64 v16, s[0:1], s0, v6
	ds_write_b128 v208, v[44:47] offset:57344
	s_nop 0
	v_addc_co_u32_e64 v17, s[0:1], 0, v7, s[0:1]
	s_mov_b32 s0, 0x1c000
	ds_write_b128 v213, v[48:51] offset:57344
	v_add_co_u32_e64 v18, s[0:1], s0, v6
	v_add_u32_e32 v216, v211, v210
	s_nop 0
	v_addc_co_u32_e64 v19, s[0:1], 0, v7, s[0:1]
	global_load_dwordx4 v[174:177], v[8:9], off sc1
	global_load_dwordx4 v[166:169], v[10:11], off sc1
	global_load_dwordx4 v[170:173], v[12:13], off sc1
	global_load_dwordx4 v[142:145], v[250:251], off offset:384 nt
	global_load_dwordx4 v[150:153], v[4:5], off offset:384 nt
	global_load_dwordx4 v[138:141], v[14:15], off sc1
	global_load_dwordx4 v[146:149], v[16:17], off sc1
	global_load_dwordx4 v[134:137], v[18:19], off sc1
	s_mov_b32 s0, 0x1e000
	v_add_co_u32_e64 v8, s[0:1], s0, v6
	s_nop 1
	v_addc_co_u32_e64 v9, s[0:1], 0, v7, s[0:1]
	global_load_dwordx4 v[130:133], v[8:9], off sc1
	s_waitcnt lgkmcnt(0)
	s_barrier
	v_lshl_add_u32 v218, v206, 6, 0
	v_add_u32_e32 v217, v218, v210
	ds_read_b128 v[198:201], v216 offset:8192
	ds_read_b128 v[194:197], v216 offset:10240
	ds_read_b128 v[190:193], v216 offset:12288
	ds_read_b128 v[178:181], v216 offset:14336
	ds_read_b128 v[186:189], v217
	ds_read_b128 v[182:185], v217 offset:2048
	v_and_b32_e32 v20, 7, v0
	v_lshl_or_b32 v2, v20, 4, v2
	s_mov_b64 s[0:1], 0x2e000
	v_lshlrev_b32_e32 v212, 4, v1
	v_lshl_add_u64 v[202:203], v[6:7], 0, s[0:1]
	s_mov_b64 s[0:1], 0x290
	v_lshl_add_u64 v[4:5], s[24:25], 0, v[2:3]
	v_lshl_add_u64 v[204:205], v[4:5], 0, s[0:1]
	v_lshl_add_u64 v[252:253], v[204:205], 0, s[46:47]
	s_mov_b64 s[24:25], 0x10000
	v_mov_b32_e32 v2, v3
	v_mov_b32_e32 v4, v3
	v_mov_b32_e32 v5, v3
	v_mov_b32_e32 v6, v3
	v_mov_b32_e32 v7, v3
	v_mov_b32_e32 v8, v3
	v_mov_b32_e32 v9, v3
	v_mov_b32_e32 v10, v3
	v_mov_b32_e32 v11, v3
	v_mov_b32_e32 v12, v3
	v_mov_b32_e32 v13, v3
	v_mov_b32_e32 v14, v3
	v_mov_b32_e32 v15, v3
	v_mov_b32_e32 v16, v3
	v_mov_b32_e32 v17, v3
	v_mov_b32_e32 v18, v3
	v_mov_b32_e32 v19, v3
	v_mov_b32_e32 v20, v3
	v_mov_b32_e32 v21, v3
	v_mov_b32_e32 v22, v3
	v_mov_b32_e32 v23, v3
	v_mov_b32_e32 v24, v3
	v_mov_b32_e32 v25, v3
	v_mov_b32_e32 v26, v3
	v_mov_b32_e32 v27, v3
	v_mov_b32_e32 v28, v3
	v_mov_b32_e32 v29, v3
	v_mov_b32_e32 v30, v3
	v_mov_b32_e32 v31, v3
	v_mov_b32_e32 v32, v3
	v_mov_b32_e32 v33, v3
	v_mov_b32_e32 v34, v3
	v_mov_b32_e32 v35, v3
	v_mov_b32_e32 v36, v3
	v_mov_b32_e32 v37, v3
	v_mov_b32_e32 v38, v3
	v_mov_b32_e32 v39, v3
	v_mov_b32_e32 v40, v3
	v_mov_b32_e32 v41, v3
	v_mov_b32_e32 v42, v3
	v_mov_b32_e32 v43, v3
	v_mov_b32_e32 v44, v3
	v_mov_b32_e32 v45, v3
	v_mov_b32_e32 v46, v3
	v_mov_b32_e32 v47, v3
	v_mov_b32_e32 v48, v3
	v_mov_b32_e32 v49, v3
	v_mov_b32_e32 v50, v3
	v_mov_b32_e32 v51, v3
	v_mov_b32_e32 v52, v3
	v_mov_b32_e32 v53, v3
	v_mov_b32_e32 v54, v3
	v_mov_b32_e32 v55, v3
	v_mov_b32_e32 v71, v3
	v_mov_b32_e32 v72, v3
	v_mov_b32_e32 v73, v3
	v_mov_b32_e32 v74, v3
	v_mov_b32_e32 v75, v3
	v_mov_b32_e32 v76, v3
	v_mov_b32_e32 v77, v3
	v_mov_b32_e32 v78, v3
	v_mov_b32_e32 v79, v3
	v_mov_b32_e32 v80, v3
	v_mov_b32_e32 v81, v3
	v_mov_b32_e32 v82, v3
	v_mov_b32_e32 v83, v3
	v_mov_b32_e32 v84, v3
	v_mov_b32_e32 v85, v3
	v_mov_b32_e32 v86, v3
	v_mov_b32_e32 v87, v3
	v_mov_b32_e32 v88, v3
	v_mov_b32_e32 v89, v3
	v_mov_b32_e32 v90, v3
	v_mov_b32_e32 v91, v3
	v_mov_b32_e32 v92, v3
	v_mov_b32_e32 v93, v3
	v_mov_b32_e32 v94, v3
	v_mov_b32_e32 v95, v3
	v_mov_b32_e32 v96, v3
	v_mov_b32_e32 v97, v3
	v_mov_b32_e32 v98, v3
	v_mov_b32_e32 v99, v3
	v_mov_b32_e32 v100, v3
	v_mov_b32_e32 v101, v3
	v_mov_b32_e32 v102, v3
	v_mov_b32_e32 v103, v3
	v_mov_b32_e32 v104, v3
	v_mov_b32_e32 v105, v3
	v_mov_b32_e32 v106, v3
	v_mov_b32_e32 v107, v3
	v_mov_b32_e32 v108, v3
	v_mov_b32_e32 v109, v3
	v_mov_b32_e32 v110, v3
	v_mov_b32_e32 v111, v3
	v_mov_b32_e32 v112, v3
	v_mov_b32_e32 v113, v3
	v_mov_b32_e32 v114, v3
	v_mov_b32_e32 v115, v3
	v_mov_b32_e32 v116, v3
	v_mov_b32_e32 v117, v3
	v_mov_b32_e32 v118, v3
	v_mov_b32_e32 v119, v3
	v_mov_b32_e32 v120, v3
	v_mov_b32_e32 v121, v3
	v_mov_b32_e32 v122, v3
	v_mov_b32_e32 v123, v3
	v_mov_b32_e32 v124, v3
	v_mov_b32_e32 v125, v3
	v_mov_b32_e32 v126, v3
	v_mov_b32_e32 v127, v3
	v_mov_b32_e32 v128, v3
	v_mov_b32_e32 v129, v3
	v_and_b32_e32 v1, 63, v0
	v_add_u32_e32 v215, v211, v212
	v_add_u32_e32 v214, v218, v212
.LBB1_1:
	s_waitcnt lgkmcnt(0)
	v_mfma_f32_32x32x16_f16 v[114:129], v[198:201], v[186:189], v[114:129]
	s_mov_b32 s44, s33
	s_mov_b32 s33, s43
	v_mfma_f32_32x32x16_f16 v[98:113], v[198:201], v[182:185], v[98:113]
	v_add_u32_e32 v219, s33, v215
	ds_read_b128 v[198:201], v219 offset:8192
	ds_read_b128 v[220:223], v219 offset:10240
	ds_read_b128 v[224:227], v219 offset:12288
	ds_read_b128 v[228:231], v219 offset:14336
	v_add_u32_e32 v219, s33, v214
	ds_read_b128 v[232:235], v219
	ds_read_b128 v[236:239], v219 offset:2048
	s_waitcnt vmcnt(10)
	v_cvt_pk_f16_f32 v162, v162, v163
	v_cvt_pk_f16_f32 v163, v164, v165
	v_cvt_pk_f16_f32 v164, v154, v155
	v_cvt_pk_f16_f32 v165, v156, v157
	v_add_u32_e32 v154, s34, v209
	ds_write_b64 v154, v[162:163]
	v_add_u32_e32 v154, s34, v248
	ds_write_b64 v154, v[164:165]
	v_mfma_f32_32x32x16_f16 v[82:97], v[194:197], v[186:189], v[82:97]
	v_add_u32_e32 v154, s34, v208
	s_waitcnt vmcnt(9)
	ds_write_b128 v154, v[158:161] offset:8192
	s_waitcnt vmcnt(8)
	ds_write_b128 v154, v[174:177] offset:16384
	v_mfma_f32_32x32x16_f16 v[66:81], v[194:197], v[182:185], v[66:81]
	v_mfma_f32_32x32x16_f16 v[50:65], v[190:193], v[186:189], v[50:65]
	s_waitcnt vmcnt(7)
	ds_write_b128 v154, v[166:169] offset:24576
	s_waitcnt vmcnt(6)
	ds_write_b128 v154, v[170:173] offset:32768
	v_mfma_f32_32x32x16_f16 v[34:49], v[190:193], v[182:185], v[34:49]
	v_add_co_u32_e64 v158, s[0:1], s36, v202
	global_load_dwordx4 v[154:157], v[252:253], off offset:-144 nt
	global_load_dwordx4 v[162:165], v[204:205], off offset:-144 nt
	v_addc_co_u32_e64 v159, s[0:1], -1, v203, s[0:1]
	v_add_co_u32_e64 v166, s[0:1], s37, v202
	v_mfma_f32_32x32x16_f16 v[18:33], v[178:181], v[186:189], v[18:33]
	s_nop 0
	v_addc_co_u32_e64 v167, s[0:1], -1, v203, s[0:1]
	global_load_dwordx4 v[158:161], v[158:159], off sc1
	s_nop 0
	global_load_dwordx4 v[174:177], v[166:167], off sc1
	v_add_co_u32_e64 v166, s[0:1], s38, v202
	s_nop 1
	v_addc_co_u32_e64 v167, s[0:1], -1, v203, s[0:1]
	v_add_co_u32_e64 v170, s[0:1], s39, v202
	v_mfma_f32_32x32x16_f16 v[2:17], v[178:181], v[182:185], v[2:17]
	s_nop 0
	v_addc_co_u32_e64 v171, s[0:1], -1, v203, s[0:1]
	global_load_dwordx4 v[166:169], v[166:167], off sc1
	s_nop 0
	global_load_dwordx4 v[170:173], v[170:171], off sc1
	v_add_u32_e32 v190, s44, v216
	ds_read_b128 v[178:181], v190 offset:8192
	ds_read_b128 v[182:185], v190 offset:10240
	ds_read_b128 v[186:189], v190 offset:12288
	ds_read_b128 v[190:193], v190 offset:14336
	v_add_u32_e32 v219, s44, v217
	ds_read_b128 v[194:197], v219
	ds_read_b128 v[240:243], v219 offset:2048
	s_waitcnt lgkmcnt(12)
	v_mfma_f32_32x32x16_f16 v[114:129], v[198:201], v[232:235], v[114:129]
	s_waitcnt lgkmcnt(11)
	v_mfma_f32_32x32x16_f16 v[98:113], v[198:201], v[236:239], v[98:113]
	v_mfma_f32_32x32x16_f16 v[82:97], v[220:223], v[232:235], v[82:97]
	v_mfma_f32_32x32x16_f16 v[66:81], v[220:223], v[236:239], v[66:81]
	v_mfma_f32_32x32x16_f16 v[50:65], v[224:227], v[232:235], v[50:65]
	v_mfma_f32_32x32x16_f16 v[34:49], v[224:227], v[236:239], v[34:49]
	v_mfma_f32_32x32x16_f16 v[18:33], v[228:231], v[232:235], v[18:33]
	v_mfma_f32_32x32x16_f16 v[2:17], v[228:231], v[236:239], v[2:17]
	s_waitcnt lgkmcnt(1)
	v_mfma_f32_32x32x16_f16 v[114:129], v[178:181], v[194:197], v[114:129]
	s_waitcnt lgkmcnt(0)
	s_barrier
	s_waitcnt lgkmcnt(0)
	v_mfma_f32_32x32x16_f16 v[98:113], v[178:181], v[240:243], v[98:113]
	v_add_u32_e32 v178, s44, v215
	ds_read_b128 v[220:223], v178 offset:8192
	ds_read_b128 v[224:227], v178 offset:10240
	ds_read_b128 v[228:231], v178 offset:12288
	ds_read_b128 v[232:235], v178 offset:14336
	v_add_u32_e32 v178, s44, v214
	ds_read_b128 v[236:239], v178
	ds_read_b128 v[244:247], v178 offset:2048
	s_waitcnt vmcnt(10)
	v_cvt_pk_f16_f32 v150, v150, v151
	v_cvt_pk_f16_f32 v151, v152, v153
	v_cvt_pk_f16_f32 v152, v142, v143
	v_cvt_pk_f16_f32 v153, v144, v145
	v_add_u32_e32 v142, s33, v209
	ds_write_b64 v142, v[150:151]
	v_add_u32_e32 v142, s33, v248
	ds_write_b64 v142, v[152:153]
	v_mfma_f32_32x32x16_f16 v[82:97], v[182:185], v[194:197], v[82:97]
	v_add_u32_e32 v142, s33, v208
	s_waitcnt vmcnt(9)
	ds_write_b128 v142, v[138:141] offset:8192
	s_waitcnt vmcnt(8)
	ds_write_b128 v142, v[146:149] offset:16384
	v_mfma_f32_32x32x16_f16 v[66:81], v[182:185], v[240:243], v[66:81]
	v_mfma_f32_32x32x16_f16 v[50:65], v[186:189], v[194:197], v[50:65]
	s_waitcnt vmcnt(7)
	ds_write_b128 v142, v[134:137] offset:24576
	s_waitcnt vmcnt(6)
	ds_write_b128 v142, v[130:133] offset:32768
	v_mfma_f32_32x32x16_f16 v[34:49], v[186:189], v[240:243], v[34:49]
	v_add_co_u32_e64 v130, s[0:1], s40, v202
	global_load_dwordx4 v[142:145], v[252:253], off offset:-16 nt
	global_load_dwordx4 v[150:153], v[204:205], off offset:-16 nt
	v_addc_co_u32_e64 v131, s[0:1], -1, v203, s[0:1]
	v_add_co_u32_e64 v132, s[0:1], s41, v202
	v_mfma_f32_32x32x16_f16 v[18:33], v[190:193], v[194:197], v[18:33]
	s_nop 0
	v_addc_co_u32_e64 v133, s[0:1], -1, v203, s[0:1]
	global_load_dwordx4 v[138:141], v[130:131], off sc1
	global_load_dwordx4 v[146:149], v[132:133], off sc1
	v_add_co_u32_e64 v130, s[0:1], s42, v202
	s_nop 1
	v_addc_co_u32_e64 v131, s[0:1], -1, v203, s[0:1]
	global_load_dwordx4 v[134:137], v[130:131], off sc1
	s_nop 0
	global_load_dwordx4 v[130:133], v[202:203], off sc1
	v_mfma_f32_32x32x16_f16 v[2:17], v[190:193], v[240:243], v[2:17]
	v_add_u32_e32 v178, s34, v216
	ds_read_b128 v[198:201], v178 offset:8192
	ds_read_b128 v[194:197], v178 offset:10240
	ds_read_b128 v[190:193], v178 offset:12288
	ds_read_b128 v[178:181], v178 offset:14336
	v_add_u32_e32 v182, s34, v217
	ds_read_b128 v[186:189], v182
	ds_read_b128 v[182:185], v182 offset:2048
	s_waitcnt lgkmcnt(12)
	v_mfma_f32_32x32x16_f16 v[114:129], v[220:223], v[236:239], v[114:129]
	s_waitcnt lgkmcnt(11)
	v_mfma_f32_32x32x16_f16 v[98:113], v[220:223], v[244:247], v[98:113]
	v_mfma_f32_32x32x16_f16 v[82:97], v[224:227], v[236:239], v[82:97]
	v_mfma_f32_32x32x16_f16 v[66:81], v[224:227], v[244:247], v[66:81]
	v_mfma_f32_32x32x16_f16 v[50:65], v[228:231], v[236:239], v[50:65]
	v_mfma_f32_32x32x16_f16 v[34:49], v[228:231], v[244:247], v[34:49]
	v_mfma_f32_32x32x16_f16 v[18:33], v[232:235], v[236:239], v[18:33]
	v_mfma_f32_32x32x16_f16 v[2:17], v[232:235], v[244:247], v[2:17]
	s_waitcnt lgkmcnt(0)
	s_barrier
	s_add_i32 s35, s35, 2
	v_lshl_add_u64 v[202:203], v[202:203], 0, s[24:25]
	v_lshl_add_u64 v[204:205], v[204:205], 0, s[26:27]
	v_lshl_add_u64 v[252:253], v[252:253], 0, s[26:27]
	s_mov_b32 s43, s34
	s_cmp_gt_u32 s35, 9
	s_mov_b32 s34, s44
	s_cbranch_scc0 .LBB1_1
	s_and_b64 s[0:1], s[20:21], exec
	s_cselect_b32 s6, s6, s8
	s_cselect_b32 s7, s7, s9
	s_and_b64 s[0:1], vcc, exec
	s_cselect_b32 s1, s5, s7
	s_cselect_b32 s0, s4, s6
	v_mov_b32_e32 v202, 0x3e38aa3b
	s_waitcnt lgkmcnt(1)
	v_mfma_f32_32x32x16_f16 v[114:129], v[198:201], v[186:189], v[114:129]
	v_cndmask_b32_e32 v202, 1.0, v202, vcc
	s_waitcnt lgkmcnt(0)
	v_mfma_f32_32x32x16_f16 v[98:113], v[198:201], v[182:185], v[98:113]
	ds_read_b128 v[198:201], v215 offset:8192
	ds_read_b128 v[220:223], v215 offset:10240
	ds_read_b128 v[224:227], v215 offset:12288
	ds_read_b128 v[228:231], v215 offset:14336
	ds_read_b128 v[232:235], v214
	ds_read_b128 v[236:239], v214 offset:2048
	s_waitcnt vmcnt(10)
	v_cvt_pk_f16_f32 v162, v162, v163
	v_cvt_pk_f16_f32 v163, v164, v165
	v_cvt_pk_f16_f32 v164, v154, v155
	v_cvt_pk_f16_f32 v165, v156, v157
	v_add_u32_e32 v154, 0x14000, v209
	ds_write_b64 v154, v[162:163]
	v_add_u32_e32 v154, 0x14000, v248
	ds_write_b64 v154, v[164:165]
	v_add_u32_e32 v154, 0x14000, v213
	s_waitcnt vmcnt(9)
	ds_write_b128 v154, v[158:161]
	v_add_u32_e32 v154, 0x16000, v213
	v_mfma_f32_32x32x16_f16 v[82:97], v[194:197], v[186:189], v[82:97]
	s_waitcnt vmcnt(8)
	ds_write_b128 v154, v[174:177]
	v_mfma_f32_32x32x16_f16 v[66:81], v[194:197], v[182:185], v[66:81]
	v_add_u32_e32 v154, 0x18000, v213
	s_waitcnt vmcnt(7)
	ds_write_b128 v154, v[166:169]
	v_add_u32_e32 v154, 0x1a000, v213
	v_mfma_f32_32x32x16_f16 v[50:65], v[190:193], v[186:189], v[50:65]
	s_waitcnt vmcnt(6)
	ds_write_b128 v154, v[170:173]
	v_mfma_f32_32x32x16_f16 v[34:49], v[190:193], v[182:185], v[34:49]
	v_mfma_f32_32x32x16_f16 v[18:33], v[178:181], v[186:189], v[18:33]
	v_mfma_f32_32x32x16_f16 v[2:17], v[178:181], v[182:185], v[2:17]
	ds_read_b128 v[154:157], v216 offset:49152
	ds_read_b128 v[158:161], v216 offset:51200
	ds_read_b128 v[162:165], v216 offset:53248
	ds_read_b128 v[166:169], v216 offset:55296
	ds_read_b128 v[170:173], v217 offset:40960
	ds_read_b128 v[174:177], v217 offset:43008
	s_waitcnt lgkmcnt(12)
	v_mfma_f32_32x32x16_f16 v[114:129], v[198:201], v[232:235], v[114:129]
	s_waitcnt lgkmcnt(11)
	v_mfma_f32_32x32x16_f16 v[98:113], v[198:201], v[236:239], v[98:113]
	v_mfma_f32_32x32x16_f16 v[82:97], v[220:223], v[232:235], v[82:97]
	v_mfma_f32_32x32x16_f16 v[66:81], v[220:223], v[236:239], v[66:81]
	v_mfma_f32_32x32x16_f16 v[50:65], v[224:227], v[232:235], v[50:65]
	v_mfma_f32_32x32x16_f16 v[34:49], v[224:227], v[236:239], v[34:49]
	v_mfma_f32_32x32x16_f16 v[18:33], v[228:231], v[232:235], v[18:33]
	v_mfma_f32_32x32x16_f16 v[2:17], v[228:231], v[236:239], v[2:17]
	s_waitcnt lgkmcnt(0)
	s_barrier
	s_waitcnt lgkmcnt(1)
	v_mfma_f32_32x32x16_f16 v[114:129], v[154:157], v[170:173], v[114:129]
	s_waitcnt lgkmcnt(0)
	v_mfma_f32_32x32x16_f16 v[98:113], v[154:157], v[174:177], v[98:113]
	ds_read_b128 v[154:157], v215 offset:49152
	ds_read_b128 v[178:181], v215 offset:51200
	ds_read_b128 v[182:185], v215 offset:53248
	ds_read_b128 v[186:189], v215 offset:55296
	ds_read_b128 v[190:193], v214 offset:40960
	ds_read_b128 v[194:197], v214 offset:43008
	s_waitcnt vmcnt(4)
	v_cvt_pk_f16_f32 v150, v150, v151
	v_cvt_pk_f16_f32 v151, v152, v153
	v_cvt_pk_f16_f32 v152, v142, v143
	v_cvt_pk_f16_f32 v153, v144, v145
	ds_write_b64 v209, v[150:151]
	ds_write_b64 v248, v[152:153]
	v_mfma_f32_32x32x16_f16 v[82:97], v[158:161], v[170:173], v[82:97]
	s_waitcnt vmcnt(3)
	ds_write_b128 v208, v[138:141] offset:8192
	s_waitcnt vmcnt(2)
	ds_write_b128 v208, v[146:149] offset:16384
	v_mfma_f32_32x32x16_f16 v[66:81], v[158:161], v[174:177], v[66:81]
	v_mfma_f32_32x32x16_f16 v[50:65], v[162:165], v[170:173], v[50:65]
	s_waitcnt vmcnt(1)
	ds_write_b128 v208, v[134:137] offset:24576
	s_waitcnt vmcnt(0)
	ds_write_b128 v208, v[130:133] offset:32768
	v_mfma_f32_32x32x16_f16 v[34:49], v[162:165], v[174:177], v[34:49]
	v_mfma_f32_32x32x16_f16 v[18:33], v[166:169], v[170:173], v[18:33]
	v_mfma_f32_32x32x16_f16 v[2:17], v[166:169], v[174:177], v[2:17]
	v_add_u32_e32 v158, 0x16000, v211
	v_add_u32_e32 v142, v158, v210
	ds_read_b128 v[130:133], v142
	ds_read_b128 v[134:137], v142 offset:2048
	ds_read_b128 v[138:141], v142 offset:4096
	ds_read_b128 v[142:145], v142 offset:6144
	v_add_u32_e32 v166, 0x14000, v218
	v_add_u32_e32 v150, v166, v210
	ds_read_b128 v[146:149], v150
	ds_read_b128 v[150:153], v150 offset:2048
	s_waitcnt lgkmcnt(12)
	v_mfma_f32_32x32x16_f16 v[114:129], v[154:157], v[190:193], v[114:129]
	s_waitcnt lgkmcnt(11)
	v_mfma_f32_32x32x16_f16 v[98:113], v[154:157], v[194:197], v[98:113]
	v_mfma_f32_32x32x16_f16 v[82:97], v[178:181], v[190:193], v[82:97]
	v_mfma_f32_32x32x16_f16 v[66:81], v[178:181], v[194:197], v[66:81]
	v_mfma_f32_32x32x16_f16 v[50:65], v[182:185], v[190:193], v[50:65]
	v_mfma_f32_32x32x16_f16 v[34:49], v[182:185], v[194:197], v[34:49]
	v_mfma_f32_32x32x16_f16 v[18:33], v[186:189], v[190:193], v[18:33]
	v_mfma_f32_32x32x16_f16 v[2:17], v[186:189], v[194:197], v[2:17]
	s_waitcnt lgkmcnt(0)
	s_barrier
	s_waitcnt lgkmcnt(1)
	v_mfma_f32_32x32x16_f16 v[114:129], v[130:133], v[146:149], v[114:129]
	s_waitcnt lgkmcnt(0)
	v_mfma_f32_32x32x16_f16 v[98:113], v[130:133], v[150:153], v[98:113]
	v_add_u32_e32 v162, v158, v212
	ds_read_b128 v[130:133], v162
	ds_read_b128 v[154:157], v162 offset:2048
	ds_read_b128 v[158:161], v162 offset:4096
	ds_read_b128 v[162:165], v162 offset:6144
	v_add_u32_e32 v170, v166, v212
	ds_read_b128 v[166:169], v170
	ds_read_b128 v[170:173], v170 offset:2048
	v_mfma_f32_32x32x16_f16 v[82:97], v[134:137], v[146:149], v[82:97]
	v_mfma_f32_32x32x16_f16 v[66:81], v[134:137], v[150:153], v[66:81]
	v_mfma_f32_32x32x16_f16 v[50:65], v[138:141], v[146:149], v[50:65]
	v_mfma_f32_32x32x16_f16 v[34:49], v[138:141], v[150:153], v[34:49]
	v_mfma_f32_32x32x16_f16 v[18:33], v[142:145], v[146:149], v[18:33]
	v_mfma_f32_32x32x16_f16 v[2:17], v[142:145], v[150:153], v[2:17]
	ds_read_b128 v[134:137], v216 offset:8192
	ds_read_b128 v[138:141], v216 offset:10240
	ds_read_b128 v[142:145], v216 offset:12288
	ds_read_b128 v[146:149], v216 offset:14336
	ds_read_b128 v[150:153], v217
	ds_read_b128 v[174:177], v217 offset:2048
	s_waitcnt lgkmcnt(7)
	v_mfma_f32_32x32x16_f16 v[114:129], v[130:133], v[166:169], v[114:129]
	s_waitcnt lgkmcnt(6)
	v_mfma_f32_32x32x16_f16 v[98:113], v[130:133], v[170:173], v[98:113]
	v_mfma_f32_32x32x16_f16 v[82:97], v[154:157], v[166:169], v[82:97]
	v_mfma_f32_32x32x16_f16 v[66:81], v[154:157], v[170:173], v[66:81]
	v_mfma_f32_32x32x16_f16 v[50:65], v[158:161], v[166:169], v[50:65]
	v_mfma_f32_32x32x16_f16 v[34:49], v[158:161], v[170:173], v[34:49]
	v_mfma_f32_32x32x16_f16 v[18:33], v[162:165], v[166:169], v[18:33]
	v_mfma_f32_32x32x16_f16 v[2:17], v[162:165], v[170:173], v[2:17]
	s_waitcnt lgkmcnt(0)
	s_barrier
	s_waitcnt lgkmcnt(1)
	v_mfma_f32_32x32x16_f16 v[114:129], v[134:137], v[150:153], v[114:129]
	s_waitcnt lgkmcnt(0)
	v_mfma_f32_32x32x16_f16 v[98:113], v[134:137], v[174:177], v[98:113]
	ds_read_b128 v[130:133], v215 offset:8192
	ds_read_b128 v[134:137], v215 offset:10240
	ds_read_b128 v[154:157], v215 offset:12288
	ds_read_b128 v[158:161], v215 offset:14336
	ds_read_b128 v[162:165], v214
	ds_read_b128 v[166:169], v214 offset:2048
	v_mfma_f32_32x32x16_f16 v[82:97], v[138:141], v[150:153], v[82:97]
	v_mfma_f32_32x32x16_f16 v[66:81], v[138:141], v[174:177], v[66:81]
	v_mfma_f32_32x32x16_f16 v[50:65], v[142:145], v[150:153], v[50:65]
	v_mfma_f32_32x32x16_f16 v[34:49], v[142:145], v[174:177], v[34:49]
	v_mfma_f32_32x32x16_f16 v[18:33], v[146:149], v[150:153], v[18:33]
	v_mfma_f32_32x32x16_f16 v[2:17], v[146:149], v[174:177], v[2:17]
	s_waitcnt lgkmcnt(1)
	v_mfma_f32_32x32x16_f16 v[114:129], v[130:133], v[162:165], v[114:129]
	s_waitcnt lgkmcnt(0)
	v_mfma_f32_32x32x16_f16 v[98:113], v[130:133], v[166:169], v[98:113]
	v_mfma_f32_32x32x16_f16 v[82:97], v[134:137], v[162:165], v[82:97]
	v_mfma_f32_32x32x16_f16 v[66:81], v[134:137], v[166:169], v[66:81]
	v_mfma_f32_32x32x16_f16 v[50:65], v[154:157], v[162:165], v[50:65]
	v_mfma_f32_32x32x16_f16 v[34:49], v[154:157], v[166:169], v[34:49]
	v_mfma_f32_32x32x16_f16 v[18:33], v[158:161], v[162:165], v[18:33]
	v_mfma_f32_32x32x16_f16 v[2:17], v[158:161], v[166:169], v[2:17]
	v_lshl_or_b32 v130, v207, 2, s31
	s_waitcnt lgkmcnt(0)
	s_barrier
	v_lshlrev_b32_e32 v154, 2, v130
	global_load_dwordx4 v[134:137], v154, s[0:1]
	global_load_dwordx4 v[150:153], v154, s[0:1] offset:32
	global_load_dwordx4 v[156:159], v154, s[0:1] offset:64
	global_load_dwordx4 v[160:163], v154, s[0:1] offset:96
	global_load_dwordx4 v[164:167], v154, s[0:1] offset:128
	global_load_dwordx4 v[168:171], v154, s[0:1] offset:160
	s_movk_i32 s4, 0x410
	v_lshlrev_b32_e32 v130, 1, v130
	v_mul_lo_u32 v131, v206, s4
	v_add3_u32 v155, 0, v130, v131
	global_load_dwordx4 v[172:175], v154, s[0:1] offset:192
	global_load_dwordx4 v[146:149], v154, s[0:1] offset:224
	global_load_dwordx4 v[142:145], v154, s[0:1] offset:256
	global_load_dwordx4 v[130:133], v154, s[0:1] offset:288
	global_load_dwordx4 v[138:141], v154, s[0:1] offset:320
	v_add_u32_e32 v176, 0x8000, v155
	s_waitcnt vmcnt(10)
	v_pk_add_f32 v[114:115], v[134:135], v[114:115]
	v_pk_add_f32 v[116:117], v[136:137], v[116:117]
	v_pk_add_f32 v[98:99], v[134:135], v[98:99]
	v_pk_add_f32 v[100:101], v[136:137], v[100:101]
	s_waitcnt vmcnt(9)
	v_pk_add_f32 v[118:119], v[150:151], v[118:119]
	v_pk_add_f32 v[120:121], v[152:153], v[120:121]
	s_waitcnt vmcnt(6)
	v_pk_add_f32 v[82:83], v[164:165], v[82:83]
	v_pk_add_f32 v[84:85], v[166:167], v[84:85]
	v_pk_add_f32 v[66:67], v[164:165], v[66:67]
	v_pk_add_f32 v[68:69], v[166:167], v[68:69]
	s_waitcnt vmcnt(5)
	v_pk_add_f32 v[70:71], v[168:169], v[70:71]
	v_pk_add_f32 v[72:73], v[170:171], v[72:73]
	v_pk_add_f32 v[102:103], v[150:151], v[102:103]
	v_pk_add_f32 v[104:105], v[152:153], v[104:105]
	v_pk_add_f32 v[122:123], v[156:157], v[122:123]
	v_pk_add_f32 v[124:125], v[158:159], v[124:125]
	v_pk_add_f32 v[106:107], v[156:157], v[106:107]
	v_pk_add_f32 v[108:109], v[158:159], v[108:109]
	v_pk_add_f32 v[126:127], v[160:161], v[126:127]
	v_pk_add_f32 v[128:129], v[162:163], v[128:129]
	v_pk_add_f32 v[110:111], v[160:161], v[110:111]
	v_pk_add_f32 v[112:113], v[162:163], v[112:113]
	v_pk_add_f32 v[86:87], v[168:169], v[86:87]
	v_pk_mul_f32 v[114:115], v[202:203], v[114:115] op_sel_hi:[0,1]
	v_pk_mul_f32 v[116:117], v[202:203], v[116:117] op_sel_hi:[0,1]
	v_pk_mul_f32 v[98:99], v[202:203], v[98:99] op_sel_hi:[0,1]
	v_pk_mul_f32 v[100:101], v[202:203], v[100:101] op_sel_hi:[0,1]
	v_pk_mul_f32 v[118:119], v[202:203], v[118:119] op_sel_hi:[0,1]
	v_pk_mul_f32 v[120:121], v[202:203], v[120:121] op_sel_hi:[0,1]
	v_pk_mul_f32 v[82:83], v[202:203], v[82:83] op_sel_hi:[0,1]
	v_pk_mul_f32 v[84:85], v[202:203], v[84:85] op_sel_hi:[0,1]
	v_pk_mul_f32 v[66:67], v[202:203], v[66:67] op_sel_hi:[0,1]
	v_pk_mul_f32 v[68:69], v[202:203], v[68:69] op_sel_hi:[0,1]
	v_pk_add_f32 v[88:89], v[170:171], v[88:89]
	v_pk_mul_f32 v[70:71], v[202:203], v[70:71] op_sel_hi:[0,1]
	v_pk_mul_f32 v[72:73], v[202:203], v[72:73] op_sel_hi:[0,1]
	v_pk_mul_f32 v[102:103], v[202:203], v[102:103] op_sel_hi:[0,1]
	v_pk_mul_f32 v[104:105], v[202:203], v[104:105] op_sel_hi:[0,1]
	v_pk_mul_f32 v[122:123], v[202:203], v[122:123] op_sel_hi:[0,1]
	v_pk_mul_f32 v[124:125], v[202:203], v[124:125] op_sel_hi:[0,1]
	v_pk_mul_f32 v[106:107], v[202:203], v[106:107] op_sel_hi:[0,1]
	v_pk_mul_f32 v[108:109], v[202:203], v[108:109] op_sel_hi:[0,1]
	v_pk_mul_f32 v[126:127], v[202:203], v[126:127] op_sel_hi:[0,1]
	v_pk_mul_f32 v[128:129], v[202:203], v[128:129] op_sel_hi:[0,1]
	v_pk_mul_f32 v[110:111], v[202:203], v[110:111] op_sel_hi:[0,1]
	v_pk_mul_f32 v[112:113], v[202:203], v[112:113] op_sel_hi:[0,1]
	v_pk_mul_f32 v[86:87], v[202:203], v[86:87] op_sel_hi:[0,1]
	v_cvt_pk_f16_f32 v114, v114, v115
	v_cvt_pk_f16_f32 v115, v116, v117
	v_cvt_pk_f16_f32 v98, v98, v99
	v_cvt_pk_f16_f32 v99, v100, v101
	v_cvt_pk_f16_f32 v100, v118, v119
	v_cvt_pk_f16_f32 v101, v120, v121
	v_cvt_pk_f16_f32 v82, v82, v83
	v_cvt_pk_f16_f32 v83, v84, v85
	v_cvt_pk_f16_f32 v84, v66, v67
	v_cvt_pk_f16_f32 v85, v68, v69
	v_pk_mul_f32 v[88:89], v[202:203], v[88:89] op_sel_hi:[0,1]
	v_cvt_pk_f16_f32 v70, v70, v71
	v_cvt_pk_f16_f32 v71, v72, v73
	v_cvt_pk_f16_f32 v102, v102, v103
	v_cvt_pk_f16_f32 v103, v104, v105
	v_cvt_pk_f16_f32 v104, v122, v123
	v_cvt_pk_f16_f32 v105, v124, v125
	v_cvt_pk_f16_f32 v106, v106, v107
	v_cvt_pk_f16_f32 v107, v108, v109
	v_cvt_pk_f16_f32 v108, v126, v127
	v_cvt_pk_f16_f32 v109, v128, v129
	v_cvt_pk_f16_f32 v110, v110, v111
	v_cvt_pk_f16_f32 v111, v112, v113
	v_cvt_pk_f16_f32 v86, v86, v87
	ds_write2_b64 v155, v[114:115], v[100:101] offset1:2
	ds_write2_b64 v176, v[98:99], v[102:103] offset0:64 offset1:66
	ds_write2_b64 v155, v[104:105], v[108:109] offset0:4 offset1:6
	ds_write2_b64 v176, v[106:107], v[110:111] offset0:68 offset1:70
	v_cvt_pk_f16_f32 v87, v88, v89
	ds_write2_b64 v176, v[84:85], v[70:71] offset0:72 offset1:74
	s_waitcnt vmcnt(4)
	v_pk_add_f32 v[70:71], v[172:173], v[90:91]
	v_pk_add_f32 v[84:85], v[174:175], v[92:93]
	v_pk_add_f32 v[74:75], v[172:173], v[74:75]
	ds_write2_b64 v155, v[82:83], v[86:87] offset0:8 offset1:10
	v_pk_mul_f32 v[82:83], v[202:203], v[70:71] op_sel_hi:[0,1]
	v_pk_mul_f32 v[84:85], v[202:203], v[84:85] op_sel_hi:[0,1]
	v_pk_mul_f32 v[74:75], v[202:203], v[74:75] op_sel_hi:[0,1]
	global_load_dwordx4 v[66:69], v154, s[0:1] offset:352
	global_load_dwordx4 v[70:73], v154, s[0:1] offset:384
	v_cvt_pk_f16_f32 v82, v82, v83
	v_cvt_pk_f16_f32 v83, v84, v85
	v_cvt_pk_f16_f32 v84, v74, v75
	v_pk_add_f32 v[74:75], v[174:175], v[76:77]
	s_waitcnt vmcnt(5)
	v_pk_add_f32 v[78:79], v[146:147], v[78:79]
	v_pk_mul_f32 v[74:75], v[202:203], v[74:75] op_sel_hi:[0,1]
	v_cvt_pk_f16_f32 v85, v74, v75
	global_load_dwordx4 v[74:77], v154, s[0:1] offset:416
	v_pk_add_f32 v[80:81], v[148:149], v[80:81]
	v_pk_mul_f32 v[78:79], v[202:203], v[78:79] op_sel_hi:[0,1]
	v_pk_mul_f32 v[80:81], v[202:203], v[80:81] op_sel_hi:[0,1]
	v_cvt_pk_f16_f32 v78, v78, v79
	v_cvt_pk_f16_f32 v79, v80, v81
	ds_write2_b64 v176, v[84:85], v[78:79] offset0:76 offset1:78
	global_load_dwordx4 v[78:81], v154, s[0:1] offset:448
	v_pk_add_f32 v[86:87], v[146:147], v[94:95]
	v_pk_add_f32 v[88:89], v[148:149], v[96:97]
	s_waitcnt vmcnt(6)
	v_pk_add_f32 v[50:51], v[142:143], v[50:51]
	v_pk_add_f32 v[52:53], v[144:145], v[52:53]
	v_pk_add_f32 v[34:35], v[142:143], v[34:35]
	v_pk_mul_f32 v[86:87], v[202:203], v[86:87] op_sel_hi:[0,1]
	v_pk_mul_f32 v[88:89], v[202:203], v[88:89] op_sel_hi:[0,1]
	v_pk_mul_f32 v[50:51], v[202:203], v[50:51] op_sel_hi:[0,1]
	v_pk_mul_f32 v[52:53], v[202:203], v[52:53] op_sel_hi:[0,1]
	v_pk_mul_f32 v[34:35], v[202:203], v[34:35] op_sel_hi:[0,1]
	v_cvt_pk_f16_f32 v86, v86, v87
	v_cvt_pk_f16_f32 v87, v88, v89
	v_cvt_pk_f16_f32 v50, v50, v51
	v_cvt_pk_f16_f32 v51, v52, v53
	v_cvt_pk_f16_f32 v52, v34, v35
	v_pk_add_f32 v[34:35], v[144:145], v[36:37]
	ds_write2_b64 v155, v[82:83], v[86:87] offset0:12 offset1:14
	v_pk_mul_f32 v[82:83], v[202:203], v[34:35] op_sel_hi:[0,1]
	global_load_dwordx4 v[34:37], v154, s[0:1] offset:480
	s_waitcnt vmcnt(6)
	v_pk_add_f32 v[38:39], v[130:131], v[38:39]
	v_pk_add_f32 v[40:41], v[132:133], v[40:41]
	v_pk_mul_f32 v[38:39], v[202:203], v[38:39] op_sel_hi:[0,1]
	v_pk_mul_f32 v[40:41], v[202:203], v[40:41] op_sel_hi:[0,1]
	v_cvt_pk_f16_f32 v53, v82, v83
	v_cvt_pk_f16_f32 v38, v38, v39
	v_cvt_pk_f16_f32 v39, v40, v41
	ds_write2_b64 v176, v[52:53], v[38:39] offset0:80 offset1:82
	s_waitcnt vmcnt(5)
	v_pk_add_f32 v[38:39], v[138:139], v[58:59]
	v_pk_add_f32 v[40:41], v[140:141], v[60:61]
	v_pk_mul_f32 v[38:39], v[202:203], v[38:39] op_sel_hi:[0,1]
	v_pk_mul_f32 v[40:41], v[202:203], v[40:41] op_sel_hi:[0,1]
	v_cvt_pk_f16_f32 v38, v38, v39
	v_cvt_pk_f16_f32 v39, v40, v41
	v_pk_add_f32 v[40:41], v[138:139], v[42:43]
	v_pk_add_f32 v[42:43], v[140:141], v[44:45]
	v_pk_mul_f32 v[40:41], v[202:203], v[40:41] op_sel_hi:[0,1]
	v_pk_mul_f32 v[42:43], v[202:203], v[42:43] op_sel_hi:[0,1]
	v_cvt_pk_f16_f32 v40, v40, v41
	v_cvt_pk_f16_f32 v41, v42, v43
	v_pk_add_f32 v[54:55], v[130:131], v[54:55]
	v_pk_add_f32 v[56:57], v[132:133], v[56:57]
	v_pk_mul_f32 v[54:55], v[202:203], v[54:55] op_sel_hi:[0,1]
	v_pk_mul_f32 v[56:57], v[202:203], v[56:57] op_sel_hi:[0,1]
	v_cmp_gt_u32_e64 s[0:1], 8, v0
	v_cvt_pk_f16_f32 v54, v54, v55
	v_cvt_pk_f16_f32 v55, v56, v57
	s_and_b64 s[6:7], s[20:21], s[0:1]
	ds_write2_b64 v155, v[50:51], v[54:55] offset0:16 offset1:18
	s_waitcnt vmcnt(4)
	v_pk_add_f32 v[42:43], v[66:67], v[62:63]
	s_waitcnt vmcnt(3)
	v_pk_add_f32 v[18:19], v[70:71], v[18:19]
	v_pk_add_f32 v[20:21], v[72:73], v[20:21]
	v_pk_add_f32 v[2:3], v[70:71], v[2:3]
	v_pk_add_f32 v[4:5], v[72:73], v[4:5]
	v_pk_mul_f32 v[18:19], v[202:203], v[18:19] op_sel_hi:[0,1]
	v_pk_mul_f32 v[20:21], v[202:203], v[20:21] op_sel_hi:[0,1]
	v_pk_mul_f32 v[2:3], v[202:203], v[2:3] op_sel_hi:[0,1]
	v_pk_mul_f32 v[4:5], v[202:203], v[4:5] op_sel_hi:[0,1]
	v_cvt_pk_f16_f32 v18, v18, v19
	v_cvt_pk_f16_f32 v19, v20, v21
	v_cvt_pk_f16_f32 v2, v2, v3
	v_cvt_pk_f16_f32 v3, v4, v5
	s_waitcnt vmcnt(2)
	v_pk_add_f32 v[4:5], v[74:75], v[22:23]
	v_pk_add_f32 v[20:21], v[76:77], v[24:25]
	v_pk_mul_f32 v[4:5], v[202:203], v[4:5] op_sel_hi:[0,1]
	v_pk_mul_f32 v[20:21], v[202:203], v[20:21] op_sel_hi:[0,1]
	v_cvt_pk_f16_f32 v4, v4, v5
	v_cvt_pk_f16_f32 v5, v20, v21
	ds_write2_b64 v155, v[18:19], v[4:5] offset0:24 offset1:26
	v_pk_add_f32 v[4:5], v[74:75], v[6:7]
	v_pk_add_f32 v[6:7], v[76:77], v[8:9]
	v_pk_mul_f32 v[4:5], v[202:203], v[4:5] op_sel_hi:[0,1]
	v_pk_mul_f32 v[6:7], v[202:203], v[6:7] op_sel_hi:[0,1]
	v_cvt_pk_f16_f32 v4, v4, v5
	v_cvt_pk_f16_f32 v5, v6, v7
	ds_write2_b64 v176, v[2:3], v[4:5] offset0:88 offset1:90
	s_waitcnt vmcnt(1)
	v_pk_add_f32 v[2:3], v[78:79], v[26:27]
	v_pk_add_f32 v[4:5], v[80:81], v[28:29]
	v_pk_mul_f32 v[2:3], v[202:203], v[2:3] op_sel_hi:[0,1]
	v_pk_mul_f32 v[4:5], v[202:203], v[4:5] op_sel_hi:[0,1]
	v_cvt_pk_f16_f32 v2, v2, v3
	v_cvt_pk_f16_f32 v3, v4, v5
	v_pk_add_f32 v[4:5], v[78:79], v[10:11]
	v_pk_add_f32 v[6:7], v[80:81], v[12:13]
	v_pk_mul_f32 v[4:5], v[202:203], v[4:5] op_sel_hi:[0,1]
	v_pk_mul_f32 v[6:7], v[202:203], v[6:7] op_sel_hi:[0,1]
	v_pk_add_f32 v[44:45], v[68:69], v[64:65]
	v_cvt_pk_f16_f32 v4, v4, v5
	v_cvt_pk_f16_f32 v5, v6, v7
	s_waitcnt vmcnt(0)
	v_pk_add_f32 v[6:7], v[34:35], v[30:31]
	v_pk_add_f32 v[8:9], v[36:37], v[32:33]
	v_pk_mul_f32 v[42:43], v[202:203], v[42:43] op_sel_hi:[0,1]
	v_pk_mul_f32 v[44:45], v[202:203], v[44:45] op_sel_hi:[0,1]
	v_pk_mul_f32 v[6:7], v[202:203], v[6:7] op_sel_hi:[0,1]
	v_pk_mul_f32 v[8:9], v[202:203], v[8:9] op_sel_hi:[0,1]
	v_cvt_pk_f16_f32 v42, v42, v43
	v_cvt_pk_f16_f32 v43, v44, v45
	v_cvt_pk_f16_f32 v6, v6, v7
	v_cvt_pk_f16_f32 v7, v8, v9
	ds_write2_b64 v155, v[38:39], v[42:43] offset0:20 offset1:22
	v_pk_add_f32 v[38:39], v[66:67], v[46:47]
	v_pk_add_f32 v[42:43], v[68:69], v[48:49]
	ds_write2_b64 v155, v[2:3], v[6:7] offset0:28 offset1:30
	v_pk_add_f32 v[2:3], v[34:35], v[14:15]
	v_pk_add_f32 v[6:7], v[36:37], v[16:17]
	v_pk_mul_f32 v[38:39], v[202:203], v[38:39] op_sel_hi:[0,1]
	v_pk_mul_f32 v[42:43], v[202:203], v[42:43] op_sel_hi:[0,1]
	v_pk_mul_f32 v[2:3], v[202:203], v[2:3] op_sel_hi:[0,1]
	v_pk_mul_f32 v[6:7], v[202:203], v[6:7] op_sel_hi:[0,1]
	v_cvt_pk_f16_f32 v38, v38, v39
	v_cvt_pk_f16_f32 v39, v42, v43
	v_cvt_pk_f16_f32 v2, v2, v3
	v_cvt_pk_f16_f32 v3, v6, v7
	ds_write2_b64 v176, v[40:41], v[38:39] offset0:84 offset1:86
	ds_write2_b64 v176, v[4:5], v[2:3] offset0:92 offset1:94
	s_and_saveexec_b64 s[4:5], s[6:7]
	v_lshl_add_u32 v2, v0, 2, 0
	v_add_u32_e32 v2, 0x20800, v2
	v_mov_b32_e32 v3, 0
	ds_write_b32 v2, v3
	s_or_b64 exec, exec, s[4:5]
	s_waitcnt lgkmcnt(0)
	s_barrier
	s_mov_b64 s[4:5], -1
	s_and_b64 vcc, exec, s[22:23]
	s_cbranch_vccnz .LBB1_7
	s_andn2_b64 vcc, exec, s[4:5]
	s_cbranch_vccz .LBB1_14

	.amdhsa_kernel _Z11proj_kernelPKfS0_S0_PKDF16_S0_S0_S0_PDF16_S3_S3_Pj
		.amdhsa_group_segment_fixed_size 0
		.amdhsa_private_segment_fixed_size 0
		.amdhsa_kernarg_size 88
		.amdhsa_user_sgpr_count 2
		.amdhsa_user_sgpr_dispatch_ptr 0
		.amdhsa_user_sgpr_queue_ptr 0
		.amdhsa_user_sgpr_kernarg_segment_ptr 1
		.amdhsa_user_sgpr_dispatch_id 0
		.amdhsa_user_sgpr_kernarg_preload_length 0
		.amdhsa_user_sgpr_kernarg_preload_offset 0
		.amdhsa_user_sgpr_private_segment_size 0
		.amdhsa_uses_dynamic_stack 0
		.amdhsa_enable_private_segment 0
		.amdhsa_system_sgpr_workgroup_id_x 1
		.amdhsa_system_sgpr_workgroup_id_y 0
		.amdhsa_system_sgpr_workgroup_id_z 0
		.amdhsa_system_sgpr_workgroup_info 0
		.amdhsa_system_vgpr_workitem_id 0
		.amdhsa_next_free_vgpr 256
		.amdhsa_next_free_sgpr 48
		.amdhsa_accum_offset 256
		.amdhsa_reserve_vcc 1
		.amdhsa_float_round_mode_32 0
		.amdhsa_float_round_mode_16_64 0
		.amdhsa_float_denorm_mode_32 3
		.amdhsa_float_denorm_mode_16_64 3
		.amdhsa_dx10_clamp 1
		.amdhsa_ieee_mode 1
		.amdhsa_fp16_overflow 0
		.amdhsa_tg_split 0
		.amdhsa_exception_fp_ieee_invalid_op 0
		.amdhsa_exception_fp_denorm_src 0
		.amdhsa_exception_fp_ieee_div_zero 0
		.amdhsa_exception_fp_ieee_overflow 0
		.amdhsa_exception_fp_ieee_underflow 0
		.amdhsa_exception_fp_ieee_inexact 0
		.amdhsa_exception_int_div_zero 0
	.end_amdhsa_kernel

amdhsa.kernels:
  - .agpr_count:     0
    .args:
      - .actual_access:  read_only
        .address_space:  global
        .offset:         0
        .size:           8
        .value_kind:     global_buffer
      - .actual_access:  read_only
        .address_space:  global
        .offset:         8
        .size:           8
        .value_kind:     global_buffer
      - .actual_access:  read_only
        .address_space:  global
        .offset:         16
        .size:           8
        .value_kind:     global_buffer
      - .actual_access:  write_only
        .address_space:  global
        .offset:         24
        .size:           8
        .value_kind:     global_buffer
      - .actual_access:  write_only
        .address_space:  global
        .offset:         32
        .size:           8
        .value_kind:     global_buffer
    .group_segment_fixed_size: 0
    .kernarg_segment_align: 8
    .kernarg_segment_size: 40
    .language:       OpenCL C
    .language_version:
      - 2
      - 0
    .max_flat_workgroup_size: 256
    .name:           _Z12wprep_kernelPKfS0_S0_PDF16_Pj
    .private_segment_fixed_size: 0
    .sgpr_count:     18
    .sgpr_spill_count: 0
    .symbol:         _Z12wprep_kernelPKfS0_S0_PDF16_Pj.kd
    .uniform_work_group_size: 1
    .uses_dynamic_stack: false
    .vgpr_count:     12
    .vgpr_spill_count: 0
    .wavefront_size: 64
  - .agpr_count:     0
    .args:
      - .actual_access:  read_only
        .address_space:  global
        .offset:         0
        .size:           8
        .value_kind:     global_buffer
      - .actual_access:  read_only
        .address_space:  global
        .offset:         8
        .size:           8
        .value_kind:     global_buffer
      - .actual_access:  read_only
        .address_space:  global
        .offset:         16
        .size:           8
        .value_kind:     global_buffer
      - .actual_access:  read_only
        .address_space:  global
        .offset:         24
        .size:           8
        .value_kind:     global_buffer
      - .actual_access:  read_only
        .address_space:  global
        .offset:         32
        .size:           8
        .value_kind:     global_buffer
      - .actual_access:  read_only
        .address_space:  global
        .offset:         40
        .size:           8
        .value_kind:     global_buffer
      - .actual_access:  read_only
        .address_space:  global
        .offset:         48
        .size:           8
        .value_kind:     global_buffer
      - .actual_access:  write_only
        .address_space:  global
        .offset:         56
        .size:           8
        .value_kind:     global_buffer
      - .actual_access:  write_only
        .address_space:  global
        .offset:         64
        .size:           8
        .value_kind:     global_buffer
      - .actual_access:  write_only
        .address_space:  global
        .offset:         72
        .size:           8
        .value_kind:     global_buffer
      - .address_space:  global
        .offset:         80
        .size:           8
        .value_kind:     global_buffer
    .group_segment_fixed_size: 0
    .kernarg_segment_align: 8
    .kernarg_segment_size: 88
    .language:       OpenCL C
    .language_version:
      - 2
      - 0
    .max_flat_workgroup_size: 512
    .name:           _Z11proj_kernelPKfS0_S0_PKDF16_S0_S0_S0_PDF16_S3_S3_Pj
    .private_segment_fixed_size: 0
    .sgpr_count:     54
    .sgpr_spill_count: 0
    .symbol:         _Z11proj_kernelPKfS0_S0_PKDF16_S0_S0_S0_PDF16_S3_S3_Pj.kd
    .uniform_work_group_size: 1
    .uses_dynamic_stack: false
    .vgpr_count:     256
    .vgpr_spill_count: 0
    .wavefront_size: 64
  - .agpr_count:     0
    .args:
      - .actual_access:  read_only
        .address_space:  global
        .offset:         0
        .size:           8
        .value_kind:     global_buffer
      - .address_space:  global
        .offset:         8
        .size:           8
        .value_kind:     global_buffer
      - .address_space:  global
        .offset:         16
        .size:           8
        .value_kind:     global_buffer
      - .actual_access:  read_only
        .address_space:  global
        .offset:         24
        .size:           8
        .value_kind:     global_buffer
      - .actual_access:  write_only
        .address_space:  global
        .offset:         32
        .size:           8
        .value_kind:     global_buffer
    .group_segment_fixed_size: 0
    .kernarg_segment_align: 8
    .kernarg_segment_size: 40
    .language:       OpenCL C
    .language_version:
      - 2
      - 0
    .max_flat_workgroup_size: 512
    .name:           _Z11attn_kernelPKDF16_S0_S0_PKjPf
    .private_segment_fixed_size: 0
    .sgpr_count:     43
    .sgpr_spill_count: 0
    .symbol:         _Z11attn_kernelPKDF16_S0_S0_PKjPf.kd
    .uniform_work_group_size: 1
    .uses_dynamic_stack: false
    .vgpr_count:     192
    .vgpr_spill_count: 0
    .wavefront_size: 64
